# proj: EB stores (never re-read on the fast path) made write-through (sc0 sc1) so less dirty data is left for the end-of-kernel L2 writeback
# speedup vs baseline: 1.0089x; 1.0033x over previous
.LBB0_3:
	s_andn2_b64 vcc, exec, s[12:13]
	s_cbranch_vccnz .LBB0_15
	v_lshlrev_b32_e32 v56, 2, v0
	v_mov_b32_e32 v57, 0
	s_waitcnt lgkmcnt(0)
	v_lshl_add_u64 v[2:3], s[6:7], 0, v[56:57]
	v_lshl_add_u64 v[4:5], s[16:17], 0, v[56:57]
	v_cmp_gt_u32_e32 vcc, 64, v0
	s_load_dwordx4 s[12:15], s[0:1], 0x28
	s_load_dwordx2 s[22:23], s[0:1], 0x8
	v_cndmask_b32_e32 v2, v4, v2, vcc
	v_cndmask_b32_e32 v3, v5, v3, vcc
	global_load_dword v54, v[2:3], off
	v_lshrrev_b32_e32 v2, 2, v0
	v_and_b32_e32 v70, 15, v0
	v_and_b32_e32 v55, 48, v2
	v_or_b32_e32 v66, v55, v70
	v_bfe_u32 v1, v0, 4, 2
	v_lshlrev_b32_e32 v2, 8, v66
	v_mov_b32_e32 v3, v57
	v_lshl_add_u64 v[2:3], s[8:9], 0, v[2:3]
	v_lshlrev_b32_e32 v4, 5, v1
	v_mov_b32_e32 v5, v57
	s_add_i32 s3, s3, -12
	s_lshl_b32 s18, s2, 1
	v_lshl_add_u64 v[2:3], v[2:3], 0, v[4:5]
	s_bfe_u32 s20, s2, 0x10002
	s_ashr_i32 s3, s3, 1
	s_and_b32 s18, s18, 6
	s_bfe_u32 s19, s2, 0x10003
	global_load_dwordx4 v[14:17], v[2:3], off
	v_lshl_add_u64 v[4:5], v[2:3], 0, 16
	s_mov_b64 s[8:9], 0x80
	s_or_b32 s19, s19, s18
	s_lshl_b32 s18, s3, 6
	s_mul_i32 s21, s20, 0x180
	global_load_dwordx4 v[18:21], v[4:5], off
	v_lshl_add_u64 v[4:5], v[2:3], 0, s[8:9]
	s_mov_b64 s[8:9], 0x90
	s_add_i32 s21, s18, s21
	s_lshl_b32 s20, s20, 3
	v_lshl_add_u64 v[2:3], v[2:3], 0, s[8:9]
	v_lshlrev_b32_e32 v22, 2, v55
	v_mov_b32_e32 v23, v57
	s_lshl_b32 s8, s19, 8
	global_load_dwordx4 v[6:9], v[4:5], off
	v_lshl_add_u64 v[24:25], s[10:11], 0, v[22:23]
	v_and_b32_e32 v72, 48, v0
	v_mov_b32_e32 v73, v57
	s_waitcnt lgkmcnt(0)
	s_add_u32 s8, s14, s8
	global_load_dwordx4 v[10:13], v[2:3], off
	v_lshl_add_u64 v[2:3], v[24:25], 0, v[72:73]
	s_addc_u32 s9, s15, 0
	global_load_dwordx4 v[2:5], v[2:3], off
	v_lshlrev_b32_e32 v26, 2, v70
	v_mov_b32_e32 v27, v57
	v_lshl_add_u64 v[22:23], s[8:9], 0, v[22:23]
	v_lshl_add_u64 v[24:25], v[24:25], 0, v[26:27]
	global_load_dword v68, v[24:25], off
	v_lshl_add_u64 v[22:23], v[22:23], 0, v[26:27]
	v_lshrrev_b32_e32 v71, 4, v0
	global_load_dword v67, v[22:23], off
	v_or_b32_e32 v22, s21, v71
	v_ashrrev_i32_e32 v23, 31, v22
	v_lshlrev_b64 v[22:23], 11, v[22:23]
	v_and_b32_e32 v73, 60, v56
	v_lshl_add_u64 v[22:23], s[22:23], 0, v[22:23]
	v_lshlrev_b32_e32 v56, 2, v73
	v_lshl_add_u64 v[62:63], v[22:23], 0, v[56:57]
	global_load_dwordx4 v[22:25], v[62:63], off
	s_mov_b32 s8, 0x10000
	v_add_co_u32_e32 v64, vcc, s8, v62
	v_lshlrev_b32_e32 v30, 9, v71
	s_nop 0
	v_addc_co_u32_e32 v65, vcc, 0, v63, vcc
	global_load_dwordx4 v[26:29], v[64:65], off
	v_lshl_or_b32 v30, s19, 15, v30
	v_mov_b32_e32 v31, v57
	v_lshl_add_u64 v[30:31], v[30:31], 2, s[12:13]
	v_lshl_add_u64 v[60:61], v[30:31], 0, v[56:57]
	global_load_dwordx4 v[30:33], v[60:61], off
	v_add_co_u32_e32 v58, vcc, s8, v60
	v_lshrrev_b32_e32 v56, 3, v0
	s_nop 0
	v_addc_co_u32_e32 v59, vcc, 0, v61, vcc
	global_load_dwordx4 v[34:37], v[58:59], off
	global_load_dwordx4 v[38:41], v[62:63], off offset:256
	global_load_dwordx4 v[42:45], v[64:65], off offset:256
	global_load_dwordx4 v[46:49], v[60:61], off offset:256
	global_load_dwordx4 v[50:53], v[58:59], off offset:256
	v_and_b32_e32 v69, 32, v56
	v_or_b32_e32 v56, v69, v70
	v_mul_u32_u24_e32 v70, 0x90, v71
	v_lshl_add_u32 v71, v73, 1, v70
	s_movk_i32 s8, 0x90
	s_or_b32 s12, s19, s20
	s_lshl_b32 s13, s12, 4
	v_cmp_lt_u32_e32 vcc, 63, v0
	s_waitcnt vmcnt(7)
	v_cvt_f16_f32_e32 v22, v22
	v_cvt_f16_f32_e32 v25, v25
	v_cvt_pk_f16_f32 v23, v23, v24
	v_pack_b32_f16 v74, v22, v23
	v_alignbit_b32 v75, v25, v23, 16
	global_load_dwordx4 v[22:25], v[62:63], off offset:512
	s_waitcnt vmcnt(7)
	v_cvt_f16_f32_e32 v26, v26
	v_cvt_f16_f32_e32 v73, v29
	v_cvt_pk_f16_f32 v70, v27, v28
	v_pack_b32_f16 v76, v26, v70
	global_load_dwordx4 v[26:29], v[64:65], off offset:512
	s_waitcnt vmcnt(7)
	v_cvt_f16_f32_e32 v30, v30
	v_alignbit_b32 v77, v73, v70, 16
	v_cvt_f16_f32_e32 v73, v33
	s_waitcnt vmcnt(6)
	v_cvt_f16_f32_e32 v34, v34
	v_cvt_f16_f32_e32 v37, v37
	v_cvt_pk_f16_f32 v70, v31, v32
	ds_write2st64_b64 v71, v[74:75], v[76:77] offset1:9
	v_pack_b32_f16 v74, v30, v70
	global_load_dwordx4 v[30:33], v[60:61], off offset:512
	v_cvt_pk_f16_f32 v35, v35, v36
	v_alignbit_b32 v75, v73, v70, 16
	v_pack_b32_f16 v34, v34, v35
	v_alignbit_b32 v35, v37, v35, 16
	ds_write2st64_b64 v71, v[74:75], v[34:35] offset0:54 offset1:63
	global_load_dwordx4 v[34:37], v[58:59], off offset:512
	v_mad_u32_u24 v70, v56, s8, v72
	s_waitcnt lgkmcnt(0)
	s_barrier
	ds_read_b128 v[74:77], v70
	s_waitcnt vmcnt(7)
	v_cvt_f16_f32_e32 v38, v38
	v_cvt_f16_f32_e32 v41, v41
	v_cvt_pk_f16_f32 v39, v39, v40
	v_mad_u32_u24 v72, v66, s8, v72
	v_pack_b32_f16 v38, v38, v39
	v_alignbit_b32 v39, v41, v39, 16
	s_waitcnt vmcnt(6)
	v_cvt_f16_f32_e32 v40, v42
	v_cvt_f16_f32_e32 v41, v45
	ds_read_b128 v[78:81], v72 offset:27648
	ds_read_b128 v[82:85], v70 offset:64
	ds_read_b128 v[86:89], v72 offset:27712
	v_cvt_pk_f16_f32 v42, v43, v44
	s_waitcnt lgkmcnt(2)
	v_mfma_f32_16x16x32_f16 v[74:77], v[74:77], v[78:81], 0
	ds_read_b128 v[90:93], v70 offset:2304
	ds_read_b128 v[94:97], v70 offset:2368
	v_pack_b32_f16 v40, v40, v42
	v_alignbit_b32 v41, v41, v42, 16
	global_load_dwordx4 v[42:45], v[62:63], off offset:768
	s_waitcnt lgkmcnt(2)
	v_mfma_f32_16x16x32_f16 v[74:77], v[82:85], v[86:89], v[74:77]
	s_waitcnt vmcnt(6)
	v_cvt_f16_f32_e32 v46, v46
	v_cvt_pk_f16_f32 v47, v47, v48
	v_cvt_f16_f32_e32 v48, v49
	s_waitcnt vmcnt(5)
	v_cvt_f16_f32_e32 v73, v50
	v_cvt_f16_f32_e32 v84, v53
	v_cvt_pk_f16_f32 v85, v51, v52
	global_load_dwordx4 v[50:53], v[64:65], off offset:768
	v_pack_b32_f16 v82, v46, v47
	v_alignbit_b32 v83, v48, v47, 16
	global_load_dwordx4 v[46:49], v[60:61], off offset:768
	ds_write2st64_b64 v71, v[38:39], v[40:41] offset0:18 offset1:27
	v_pack_b32_f16 v38, v73, v85
	v_alignbit_b32 v39, v84, v85, 16
	ds_write2st64_b64 v71, v[82:83], v[38:39] offset0:72 offset1:81
	global_load_dwordx4 v[38:41], v[58:59], off offset:768
	s_waitcnt lgkmcnt(0)
	s_barrier
	ds_read_b128 v[82:85], v70 offset:9216
	v_mfma_f32_16x16x32_f16 v[78:81], v[90:93], v[78:81], 0
	s_waitcnt vmcnt(7)
	v_cvt_f16_f32_e32 v22, v22
	v_mfma_f32_16x16x32_f16 v[78:81], v[94:97], v[86:89], v[78:81]
	ds_read_b128 v[86:89], v72 offset:36864
	ds_read_b128 v[90:93], v70 offset:9280
	ds_read_b128 v[94:97], v72 offset:36928
	v_cvt_f16_f32_e32 v25, v25
	v_cvt_pk_f16_f32 v23, v23, v24
	s_waitcnt lgkmcnt(2)
	v_mfma_f32_16x16x32_f16 v[74:77], v[82:85], v[86:89], v[74:77]
	ds_read_b128 v[82:85], v70 offset:11520
	ds_read_b128 v[98:101], v70 offset:11584
	s_waitcnt vmcnt(6)
	v_cvt_f16_f32_e32 v24, v29
	s_waitcnt vmcnt(4)
	v_cvt_f16_f32_e32 v34, v34
	s_waitcnt lgkmcnt(1)
	v_mfma_f32_16x16x32_f16 v[78:81], v[82:85], v[86:89], v[78:81]
	v_pack_b32_f16 v82, v22, v23
	v_cvt_f16_f32_e32 v22, v26
	v_alignbit_b32 v83, v25, v23, 16
	v_cvt_pk_f16_f32 v23, v27, v28
	v_alignbit_b32 v85, v24, v23, 16
	v_pack_b32_f16 v84, v22, v23
	v_cvt_f16_f32_e32 v26, v30
	v_cvt_f16_f32_e32 v27, v33
	global_load_dwordx4 v[22:25], v[62:63], off offset:1024
	v_cvt_pk_f16_f32 v28, v31, v32
	v_cvt_pk_f16_f32 v35, v35, v36
	v_cvt_f16_f32_e32 v36, v37
	v_pack_b32_f16 v86, v26, v28
	v_alignbit_b32 v87, v27, v28, 16
	global_load_dwordx4 v[26:29], v[64:65], off offset:1024
	v_pack_b32_f16 v34, v34, v35
	v_alignbit_b32 v35, v36, v35, 16
	global_load_dwordx4 v[30:33], v[60:61], off offset:1024
	ds_write2st64_b64 v71, v[86:87], v[34:35] offset0:54 offset1:63
	global_load_dwordx4 v[34:37], v[58:59], off offset:1024
	ds_write2st64_b64 v71, v[82:83], v[84:85] offset1:9
	s_waitcnt lgkmcnt(0)
	s_barrier
	ds_read_b128 v[82:85], v70
	v_mfma_f32_16x16x32_f16 v[74:77], v[90:93], v[94:97], v[74:77]
	s_waitcnt vmcnt(7)
	v_cvt_f16_f32_e32 v42, v42
	v_cvt_pk_f16_f32 v43, v43, v44
	v_cvt_f16_f32_e32 v45, v45
	v_mfma_f32_16x16x32_f16 v[78:81], v[98:101], v[94:97], v[78:81]
	ds_read_b128 v[86:89], v72 offset:27648
	ds_read_b128 v[90:93], v70 offset:64
	ds_read_b128 v[94:97], v72 offset:27712
	s_waitcnt vmcnt(6)
	v_cvt_pk_f16_f32 v44, v51, v52
	s_waitcnt vmcnt(5)
	v_cvt_pk_f16_f32 v47, v47, v48
	s_waitcnt lgkmcnt(2)
	v_mfma_f32_16x16x32_f16 v[74:77], v[82:85], v[86:89], v[74:77]
	ds_read_b128 v[82:85], v70 offset:2304
	ds_read_b128 v[98:101], v70 offset:2368
	s_waitcnt vmcnt(4)
	v_cvt_pk_f16_f32 v48, v39, v40
	s_waitcnt vmcnt(3)
	v_cvt_f16_f32_e32 v22, v22
	s_waitcnt lgkmcnt(1)
	v_mfma_f32_16x16x32_f16 v[78:81], v[82:85], v[86:89], v[78:81]
	v_pack_b32_f16 v82, v42, v43
	v_cvt_f16_f32_e32 v42, v50
	v_alignbit_b32 v83, v45, v43, 16
	v_cvt_f16_f32_e32 v43, v53
	v_mfma_f32_16x16x32_f16 v[74:77], v[90:93], v[94:97], v[74:77]
	v_pack_b32_f16 v50, v42, v44
	v_cvt_f16_f32_e32 v42, v46
	v_alignbit_b32 v51, v43, v44, 16
	v_cvt_f16_f32_e32 v46, v49
	ds_write2st64_b64 v71, v[82:83], v[50:51] offset0:18 offset1:27
	v_pack_b32_f16 v52, v42, v47
	global_load_dwordx4 v[42:45], v[62:63], off offset:1280
	v_alignbit_b32 v53, v46, v47, 16
	v_cvt_f16_f32_e32 v46, v38
	v_cvt_f16_f32_e32 v47, v41
	global_load_dwordx4 v[38:41], v[64:65], off offset:1280
	s_waitcnt lgkmcnt(1)
	v_mfma_f32_16x16x32_f16 v[78:81], v[98:101], v[94:97], v[78:81]
	v_pack_b32_f16 v84, v46, v48
	v_alignbit_b32 v85, v47, v48, 16
	global_load_dwordx4 v[46:49], v[60:61], off offset:1280
	ds_write2st64_b64 v71, v[52:53], v[84:85] offset0:72 offset1:81
	global_load_dwordx4 v[50:53], v[58:59], off offset:1280
	s_waitcnt lgkmcnt(0)
	s_barrier
	ds_read_b128 v[82:85], v70 offset:9216
	ds_read_b128 v[86:89], v72 offset:36864
	ds_read_b128 v[90:93], v70 offset:9280
	ds_read_b128 v[94:97], v72 offset:36928
	s_waitcnt lgkmcnt(2)
	v_mfma_f32_16x16x32_f16 v[74:77], v[82:85], v[86:89], v[74:77]
	ds_read_b128 v[82:85], v70 offset:11520
	ds_read_b128 v[98:101], v70 offset:11584
	v_cvt_pk_f16_f32 v73, v23, v24
	s_waitcnt vmcnt(6)
	v_cvt_f16_f32_e32 v26, v26
	s_waitcnt lgkmcnt(1)
	v_mfma_f32_16x16x32_f16 v[78:81], v[82:85], v[86:89], v[78:81]
	v_cvt_f16_f32_e32 v83, v25
	v_pack_b32_f16 v82, v22, v73
	global_load_dwordx4 v[22:25], v[62:63], off offset:1536
	v_cvt_f16_f32_e32 v85, v29
	v_alignbit_b32 v83, v83, v73, 16
	v_cvt_pk_f16_f32 v73, v27, v28
	v_pack_b32_f16 v84, v26, v73
	global_load_dwordx4 v[26:29], v[64:65], off offset:1536
	v_alignbit_b32 v85, v85, v73, 16
	s_waitcnt vmcnt(7)
	v_cvt_f16_f32_e32 v73, v30
	v_cvt_f16_f32_e32 v87, v33
	s_waitcnt vmcnt(6)
	v_cvt_f16_f32_e32 v34, v34
	v_cvt_pk_f16_f32 v88, v31, v32
	v_cvt_pk_f16_f32 v89, v35, v36
	global_load_dwordx4 v[30:33], v[60:61], off offset:1536
	v_pack_b32_f16 v86, v73, v88
	v_alignbit_b32 v87, v87, v88, 16
	v_cvt_f16_f32_e32 v73, v37
	v_pack_b32_f16 v88, v34, v89
	global_load_dwordx4 v[34:37], v[58:59], off offset:1536
	ds_write2st64_b64 v71, v[82:83], v[84:85] offset1:9
	v_alignbit_b32 v89, v73, v89, 16
	ds_write2st64_b64 v71, v[86:87], v[88:89] offset0:54 offset1:63
	s_waitcnt lgkmcnt(0)
	s_barrier
	global_load_dwordx4 v[82:85], v[62:63], off offset:1792
	ds_read_b128 v[86:89], v70
	global_load_dwordx4 v[62:65], v[64:65], off offset:1792
	v_mfma_f32_16x16x32_f16 v[74:77], v[90:93], v[94:97], v[74:77]
	s_waitcnt vmcnt(9)
	v_cvt_pk_f16_f32 v73, v43, v44
	v_mfma_f32_16x16x32_f16 v[78:81], v[98:101], v[94:97], v[78:81]
	ds_read_b128 v[90:93], v72 offset:27648
	ds_read_b128 v[94:97], v70 offset:64
	ds_read_b128 v[98:101], v72 offset:27712
	s_waitcnt vmcnt(8)
	v_cvt_f16_f32_e32 v41, v41
	s_waitcnt lgkmcnt(2)
	v_mfma_f32_16x16x32_f16 v[74:77], v[86:89], v[90:93], v[74:77]
	ds_read_b128 v[86:89], v70 offset:2304
	ds_read_b128 v[102:105], v70 offset:2368
	s_waitcnt vmcnt(7)
	v_cvt_f16_f32_e32 v46, v46
	s_waitcnt lgkmcnt(1)
	v_mfma_f32_16x16x32_f16 v[78:81], v[86:89], v[90:93], v[78:81]
	global_load_dwordx4 v[86:89], v[60:61], off offset:1792
	v_cvt_f16_f32_e32 v60, v42
	v_cvt_f16_f32_e32 v61, v45
	global_load_dwordx4 v[42:45], v[58:59], off offset:1792
	v_cvt_f16_f32_e32 v49, v49
	v_cvt_pk_f16_f32 v47, v47, v48
	v_cvt_f16_f32_e32 v90, v38
	v_pack_b32_f16 v46, v46, v47
	s_waitcnt vmcnt(8)
	v_cvt_f16_f32_e32 v48, v50
	v_alignbit_b32 v47, v49, v47, 16
	v_cvt_f16_f32_e32 v49, v53
	v_pack_b32_f16 v38, v60, v73
	v_cvt_pk_f16_f32 v91, v39, v40
	v_cvt_pk_f16_f32 v50, v51, v52
	v_alignbit_b32 v39, v61, v73, 16
	v_pack_b32_f16 v40, v90, v91
	v_alignbit_b32 v41, v41, v91, 16
	v_pack_b32_f16 v48, v48, v50
	v_alignbit_b32 v49, v49, v50, 16
	ds_write2st64_b64 v71, v[38:39], v[40:41] offset0:18 offset1:27
	s_waitcnt vmcnt(7)
	v_cvt_f16_f32_e32 v22, v22
	v_cvt_f16_f32_e32 v25, v25
	v_cvt_pk_f16_f32 v23, v23, v24
	ds_write2st64_b64 v71, v[46:47], v[48:49] offset0:72 offset1:81
	v_pack_b32_f16 v58, v22, v23
	s_waitcnt vmcnt(6)
	v_cvt_f16_f32_e32 v22, v26
	v_alignbit_b32 v59, v25, v23, 16
	v_cvt_pk_f16_f32 v23, v27, v28
	v_cvt_f16_f32_e32 v24, v29
	v_pack_b32_f16 v60, v22, v23
	s_waitcnt lgkmcnt(0)
	s_barrier
	s_waitcnt vmcnt(5)
	v_cvt_f16_f32_e32 v22, v30
	v_cvt_f16_f32_e32 v25, v33
	v_alignbit_b32 v61, v24, v23, 16
	v_cvt_pk_f16_f32 v23, v31, v32
	v_pack_b32_f16 v90, v22, v23
	s_waitcnt vmcnt(4)
	v_cvt_f16_f32_e32 v26, v34
	v_cvt_f16_f32_e32 v27, v37
	v_cvt_pk_f16_f32 v28, v35, v36
	v_alignbit_b32 v91, v25, v23, 16
	v_mfma_f32_16x16x32_f16 v[22:25], v[102:105], v[98:101], v[78:81]
	s_waitcnt vmcnt(3)
	v_cvt_f16_f32_e32 v30, v82
	s_nop 0
	v_pack_b32_f16 v78, v26, v28
	v_alignbit_b32 v79, v27, v28, 16
	ds_read_b128 v[26:29], v70 offset:9216
	v_cvt_f16_f32_e32 v31, v85
	s_waitcnt vmcnt(2)
	v_cvt_f16_f32_e32 v50, v62
	v_cvt_pk_f16_f32 v32, v83, v84
	v_cvt_pk_f16_f32 v63, v63, v64
	v_mfma_f32_16x16x32_f16 v[74:77], v[94:97], v[98:101], v[74:77]
	v_pack_b32_f16 v80, v30, v32
	v_alignbit_b32 v81, v31, v32, 16
	ds_read_b128 v[30:33], v72 offset:36864
	ds_read_b128 v[34:37], v70 offset:11520
	ds_read_b128 v[38:41], v70 offset:9280
	ds_read_b128 v[46:49], v72 offset:36928
	v_pack_b32_f16 v62, v50, v63
	ds_read_b128 v[50:53], v70 offset:11584
	s_waitcnt lgkmcnt(4)
	v_mfma_f32_16x16x32_f16 v[26:29], v[26:29], v[30:33], v[74:77]
	ds_write2st64_b64 v71, v[58:59], v[60:61] offset1:9
	ds_write2st64_b64 v71, v[90:91], v[78:79] offset0:54 offset1:63
	s_waitcnt lgkmcnt(0)
	s_barrier
	v_mfma_f32_16x16x32_f16 v[22:25], v[34:37], v[30:33], v[22:25]
	ds_read_b128 v[30:33], v70
	v_cvt_f16_f32_e32 v64, v65
	v_mfma_f32_16x16x32_f16 v[26:29], v[38:41], v[46:49], v[26:29]
	ds_read_b128 v[34:37], v70 offset:2304
	ds_read_b128 v[38:41], v72 offset:27648
	v_alignbit_b32 v63, v64, v63, 16
	v_mfma_f32_16x16x32_f16 v[22:25], v[50:53], v[46:49], v[22:25]
	ds_read_b128 v[46:49], v70 offset:64
	ds_read_b128 v[50:53], v72 offset:27712
	s_waitcnt vmcnt(1)
	v_cvt_f16_f32_e32 v58, v86
	v_cvt_f16_f32_e32 v60, v89
	s_waitcnt lgkmcnt(2)
	v_mfma_f32_16x16x32_f16 v[22:25], v[34:37], v[38:41], v[22:25]
	s_waitcnt vmcnt(0)
	v_cvt_f16_f32_e32 v36, v42
	v_cvt_f16_f32_e32 v37, v45
	v_cvt_pk_f16_f32 v59, v87, v88
	v_mfma_f32_16x16x32_f16 v[26:29], v[30:33], v[38:41], v[26:29]
	ds_read_b128 v[30:33], v70 offset:2368
	v_cvt_pk_f16_f32 v38, v43, v44
	v_pack_b32_f16 v34, v58, v59
	v_alignbit_b32 v35, v60, v59, 16
	v_pack_b32_f16 v36, v36, v38
	v_alignbit_b32 v37, v37, v38, 16
	ds_write2st64_b64 v71, v[80:81], v[62:63] offset0:18 offset1:27
	ds_write2st64_b64 v71, v[34:35], v[36:37] offset0:72 offset1:81
	s_waitcnt lgkmcnt(0)
	s_barrier
	ds_read_b128 v[34:37], v70 offset:9216
	v_mfma_f32_16x16x32_f16 v[26:29], v[46:49], v[50:53], v[26:29]
	v_mfma_f32_16x16x32_f16 v[22:25], v[30:33], v[50:53], v[22:25]
	ds_read_b128 v[30:33], v72 offset:36864
	ds_read_b128 v[38:41], v70 offset:9280
	ds_read_b128 v[42:45], v72 offset:36928
	s_waitcnt lgkmcnt(2)
	v_mfma_f32_16x16x32_f16 v[26:29], v[34:37], v[30:33], v[26:29]
	ds_read_b128 v[34:37], v70 offset:11520
	ds_read_b128 v[46:49], v70 offset:11584
	s_waitcnt vmcnt(0)
	s_waitcnt lgkmcnt(0)
	v_mfma_f32_16x16x32_f16 v[22:25], v[34:37], v[30:33], v[22:25]
	v_lshl_or_b32 v30, v1, 2, v69
	v_mul_u32_u24_e32 v30, 0x90, v30
	v_lshl_add_u32 v30, v66, 1, v30
	v_mfma_f32_16x16x32_f16 v[26:29], v[38:41], v[42:45], v[26:29]
	v_cvt_pk_f16_f32 v21, v20, v21
	v_cvt_pk_f16_f32 v20, v18, v19
	v_cvt_pk_f16_f32 v19, v16, v17
	v_mfma_f32_16x16x32_f16 v[22:25], v[46:49], v[42:45], v[22:25]
	v_cvt_pk_f16_f32 v18, v14, v15
	s_nop 2
	v_add_f32_e32 v26, v26, v67
	v_cvt_f16_f32_e32 v26, v26
	v_add_f32_e32 v27, v27, v67
	v_cvt_f16_f32_e32 v27, v27
	v_add_f32_e32 v22, v22, v67
	v_cvt_f16_f32_e32 v22, v22
	v_add_f32_e32 v23, v23, v67
	v_add_f32_e32 v28, v28, v67
	v_cvt_f16_f32_e32 v23, v23
	v_add_f32_e32 v24, v24, v67
	v_cvt_f16_f32_e32 v28, v28
	v_add_f32_e32 v29, v29, v67
	v_cvt_f16_f32_e32 v24, v24
	v_add_f32_e32 v25, v25, v67
	v_cvt_f16_f32_e32 v29, v29
	v_cvt_f16_f32_e32 v25, v25
	s_barrier
	ds_write_b16 v30, v26
	ds_write_b16 v30, v27 offset:144
	ds_write_b16 v30, v28 offset:288
	ds_write_b16 v30, v29 offset:432
	ds_write_b16 v30, v22 offset:2304
	ds_write_b16 v30, v23 offset:2448
	ds_write_b16 v30, v24 offset:2592
	ds_write_b16 v30, v25 offset:2736
	s_waitcnt lgkmcnt(0)
	s_barrier
	ds_read_b128 v[14:17], v70
	ds_read_b128 v[22:25], v70 offset:64
	v_cvt_pk_f16_f32 v13, v12, v13
	v_cvt_pk_f16_f32 v12, v10, v11
	v_cvt_pk_f16_f32 v11, v8, v9
	v_cvt_pk_f16_f32 v10, v6, v7
	s_waitcnt lgkmcnt(1)
	v_mfma_f32_16x16x32_f16 v[14:17], v[18:21], v[14:17], 0
	ds_read_b128 v[26:29], v70 offset:2304
	ds_read_b128 v[30:33], v70 offset:2368
	s_load_dwordx2 s[10:11], s[0:1], 0x70
	s_load_dwordx2 s[8:9], s[0:1], 0x98
	s_waitcnt lgkmcnt(0)
	v_mfma_f32_16x16x32_f16 v[6:9], v[10:13], v[22:25], v[14:17]
	v_or_b32_e32 v22, s18, v56
	v_ashrrev_i32_e32 v23, 31, v22
	s_nop 0
	v_lshrrev_b32_e32 v14, 2, v55
	v_or3_b32 v1, s13, v14, v1
	v_mfma_f32_16x16x32_f16 v[18:21], v[18:21], v[26:29], 0
	v_mul_u32_u24_e32 v56, 0x180, v1
	s_nop 0
	v_add_f32_e32 v1, v2, v6
	s_mov_b32 s13, 0xc2200000
	v_mov_b32_e32 v28, 0x42200000
	v_med3_f32 v1, v1, s13, v28
	v_mul_f32_e32 v1, 0x4038aa3b, v1
	v_exp_f32_e32 v6, v1
	v_add_f32_e32 v1, v3, v7
	v_med3_f32 v1, v1, s13, v28
	v_mul_f32_e32 v1, 0x4038aa3b, v1
	v_exp_f32_e32 v7, v1
	v_add_f32_e32 v1, v4, v8
	v_med3_f32 v1, v1, s13, v28
	v_mul_f32_e32 v1, 0x4038aa3b, v1
	v_exp_f32_e32 v8, v1
	v_add_f32_e32 v1, v5, v9
	v_med3_f32 v1, v1, s13, v28
	v_mul_f32_e32 v1, 0x4038aa3b, v1
	v_exp_f32_e32 v9, v1
	v_cvt_f16_f32_e32 v1, v6
	v_lshl_add_u64 v[24:25], v[56:57], 0, v[22:23]
	v_lshl_add_u64 v[14:15], v[24:25], 4, s[10:11]
	global_store_dwordx4 v[14:15], v[6:9], off sc0 sc1
	v_pack_b32_f16 v14, 1.0, v1
	v_cvt_f16_f32_e32 v1, v9
	v_mfma_f32_16x16x32_f16 v[10:13], v[10:13], v[30:33], v[18:21]
	v_mul_f32_e32 v16, v6, v7
	v_mov_b32_e32 v17, v8
	v_pk_mul_f32 v[26:27], v[6:7], v[8:9] op_sel_hi:[1,0]
	v_mov_b32_e32 v20, v9
	v_pk_mul_f32 v[18:19], v[6:7], v[20:21] op_sel_hi:[1,0]
	v_mul_f32_e32 v23, v8, v16
	v_cvt_pk_f16_f32 v15, v7, v16
	v_cvt_pk_f16_f32 v19, v18, v19
	v_pk_mul_f32 v[16:17], v[20:21], v[16:17] op_sel_hi:[0,1]
	v_pk_mul_f32 v[20:21], v[20:21], v[26:27] op_sel_hi:[0,1]
	v_pack_b32_f16 v18, v1, v19
	v_cvt_pk_f16_f32 v1, v16, v17
	v_cvt_pk_f16_f32 v21, v20, v21
	v_alignbit_b32 v19, v1, v19, 16
	v_alignbit_b32 v20, v21, v1, 16
	v_add_f32_e32 v1, v2, v10
	v_med3_f32 v1, v1, s13, v28
	v_mul_f32_e32 v1, 0x4038aa3b, v1
	v_exp_f32_e32 v2, v1
	v_add_f32_e32 v1, v3, v11
	v_med3_f32 v1, v1, s13, v28
	v_mul_f32_e32 v1, 0x4038aa3b, v1
	v_exp_f32_e32 v3, v1
	v_add_f32_e32 v1, v4, v12
	v_med3_f32 v1, v1, s13, v28
	v_mul_f32_e32 v1, 0x4038aa3b, v1
	v_exp_f32_e32 v4, v1
	v_add_f32_e32 v1, v5, v13
	v_lshlrev_b64 v[24:25], 5, v[24:25]
	v_med3_f32 v1, v1, s13, v28
	v_cvt_pk_f16_f32 v16, v8, v26
	v_cvt_pk_f16_f32 v17, v27, v23
	v_lshrrev_b32_e32 v21, 16, v21
	v_lshl_add_u64 v[24:25], s[8:9], 0, v[24:25]
	v_mul_f32_e32 v1, 0x4038aa3b, v1
	v_fma_mixhi_f16 v21, v9, v23, 0
	global_store_dwordx4 v[24:25], v[14:17], off
	global_store_dwordx4 v[24:25], v[18:21], off offset:16
	v_exp_f32_e32 v5, v1
	v_or_b32_e32 v14, 16, v22
	v_cvt_f16_f32_e32 v1, v2
	v_ashrrev_i32_e32 v15, 31, v14
	v_lshl_add_u64 v[18:19], v[56:57], 0, v[14:15]
	v_lshl_add_u64 v[10:11], v[18:19], 4, s[10:11]
	global_store_dwordx4 v[10:11], v[2:5], off sc0 sc1
	v_pack_b32_f16 v10, 1.0, v1
	v_cvt_f16_f32_e32 v1, v5
	v_mov_b32_e32 v16, v5
	v_mul_f32_e32 v12, v2, v3
	v_pk_mul_f32 v[14:15], v[2:3], v[16:17] op_sel_hi:[1,0]
	v_mov_b32_e32 v13, v4
	v_pk_mul_f32 v[20:21], v[2:3], v[4:5] op_sel_hi:[1,0]
	v_mul_f32_e32 v22, v4, v12
	v_cvt_pk_f16_f32 v11, v3, v12
	v_cvt_pk_f16_f32 v15, v14, v15
	v_pk_mul_f32 v[12:13], v[16:17], v[12:13] op_sel_hi:[0,1]
	v_pk_mul_f32 v[16:17], v[16:17], v[20:21] op_sel_hi:[0,1]
	v_pack_b32_f16 v14, v1, v15
	v_cvt_pk_f16_f32 v1, v12, v13
	v_cvt_pk_f16_f32 v17, v16, v17
	v_lshlrev_b64 v[18:19], 5, v[18:19]
	v_alignbit_b32 v15, v1, v15, 16
	v_cvt_pk_f16_f32 v12, v4, v20
	v_cvt_pk_f16_f32 v13, v21, v22
	v_alignbit_b32 v16, v17, v1, 16
	v_lshrrev_b32_e32 v17, 16, v17
	v_lshl_add_u64 v[18:19], s[8:9], 0, v[18:19]
	v_fma_mixhi_f16 v17, v5, v22, 0
	global_store_dwordx4 v[18:19], v[10:13], off
	global_store_dwordx4 v[18:19], v[14:17], off offset:16
	s_and_saveexec_b64 s[8:9], vcc
	s_xor_b64 s[8:9], exec, s[8:9]
	s_cbranch_execz .LBB0_6
	v_mbcnt_lo_u32_b32 v1, -1, 0
	v_mbcnt_hi_u32_b32 v1, -1, v1
	v_and_b32_e32 v10, 64, v1
	v_add_u32_e32 v14, 64, v10
	v_xor_b32_e32 v15, 32, v1
	v_xor_b32_e32 v16, 16, v1
	v_xor_b32_e32 v18, 8, v1
	v_xor_b32_e32 v19, 4, v1
	v_xor_b32_e32 v20, 2, v1
	v_xor_b32_e32 v21, 1, v1
